# G=200; dedicated 6112 W1; GEMM-in epilogues 800 (half WG/unit); W_out epilogues 512; phase-2 late: 1 W2 + 6 W1 tiles per WG (negative stride); GEMM1 epilogues 3968 W2
# speedup vs baseline: 1.0172x; 1.0172x over previous
.LBB0_86:
	s_cmp_lt_i32 s50, 2
	s_cselect_b64 s[6:7], -1, 0
	s_and_b64 s[0:1], s[6:7], s[2:3]
	s_andn2_b64 vcc, exec, s[0:1]
	v_writelane_b32 v254, s60, 4
	s_cbranch_vccnz .LBB0_260
	s_mov_b64 s[2:3], s[80:81]
	s_load_dwordx2 s[8:9], s[2:3], 0xa8
	s_cmpk_lg_i32 s56, 0x100
	s_cselect_b32 s0, s56, 0xc8
	s_cmp_ge_i32 s78, s0
	s_mov_b64 s[4:5], -1
	s_cbranch_scc0 .LBB0_145
	s_sub_i32 s1, s78, s0
	s_cmpk_gt_i32 s1, 0x17df
	s_cbranch_scc1 .LBB0_144
	s_sub_i32 s20, s56, s0
	s_abs_i32 s4, s20
	v_cvt_f32_u32_e32 v1, s4
	s_load_dwordx2 s[10:11], s[2:3], 0x78
	s_load_dwordx2 s[12:13], s[2:3], 0x88
	s_sub_i32 s2, s20, s1
	s_add_i32 s3, s2, 0x17df
	v_rcp_iflag_f32_e32 v1, v1
	s_sub_i32 s2, 0xffffe821, s2
	s_xor_b32 s14, s3, s20
	s_sub_i32 s5, 0, s4
	v_mul_f32_e32 v1, 0x4f7ffffe, v1
	v_cvt_u32_f32_e32 v1, v1
	s_max_i32 s2, s3, s2
	s_ashr_i32 s3, s14, 31
	v_readfirstlane_b32 s14, v1
	s_mul_i32 s5, s5, s14
	s_mul_hi_u32 s5, s14, s5
	s_add_i32 s14, s14, s5
	s_mul_hi_u32 s5, s2, s14
	s_mul_i32 s14, s5, s4
	s_sub_i32 s2, s2, s14
	s_add_i32 s14, s5, 1
	s_sub_i32 s15, s2, s4
	s_cmp_ge_u32 s2, s4
	s_cselect_b32 s5, s14, s5
	s_cselect_b32 s2, s15, s2
	s_add_i32 s14, s5, 1
	s_cmp_ge_u32 s2, s4
	s_cselect_b32 s2, s14, s5
	s_xor_b32 s2, s2, s3
	s_sub_i32 s29, s2, s3
	s_lshl_b32 s21, s29, 2
	s_add_i32 s22, s21, -1
	s_cmp_gt_i32 s29, 0
	s_cselect_b64 s[2:3], -1, 0
	s_and_b64 s[4:5], s[2:3], exec
	s_cselect_b32 s18, 0, s22
	s_ashr_i32 s4, s18, 2
	s_mul_i32 s17, s4, s20
	s_add_i32 s17, s17, s1
	s_cmpk_gt_i32 s17, 0x1fff
	s_mov_b32 s5, 0
	s_cbranch_scc0 .LBB0_91
	s_add_i32 s4, s17, 0xffffe000
	s_lshr_b32 s4, s4, 7
	s_lshl_b64 s[4:5], s[4:5], 24
	s_waitcnt lgkmcnt(0)
	s_add_u32 s14, s12, s4
	s_addc_u32 s15, s13, s5
	s_lshl_b32 s4, s17, 4
	s_and_b32 s26, s4, 0x780
	s_lshl_b32 s4, s17, 8
	s_and_b32 s16, s4, 0x700
	s_mov_b64 s[4:5], 0x800
	s_cbranch_execz .LBB0_92
	s_branch .LBB0_93

.LBB0_160:
	s_add_i32 s89, s59, -1
	s_cmp_lt_u32 s89, 8
	s_cselect_b32 s88, 1, 0
	s_cbranch_scc0 .Lp1c_skip1
	s_and_b32 s90, s89, 1
	s_lshr_b32 s91, s57, 2
	s_cmp_eq_u32 s90, s91
	s_cselect_b32 s88, 1, 0
	s_cbranch_scc0 .Lp1c_skip1
	s_lshr_b32 s89, s89, 1
	s_mul_i32 s89, s89, 200
	s_add_u32 s89, s89, s78
	s_add_u32 s89, s89, 6112
	s_cmp_lt_u32 s89, 0x2000
	s_cselect_b32 s88, 1, 0
	s_cbranch_scc0 .Lp1c_skip1
	s_lshr_b32 s90, s89, 4
	s_lshl_b32 s90, s90, 21
	s_and_b32 s91, s89, 15
	s_lshl_b32 s92, s91, 10
	s_or_b32 s90, s90, s92
	s_lshl_b32 s92, s57, 7
	s_or_b32 s90, s90, s92
	s_add_u32 s84, s82, s90
	s_addc_u32 s85, s83, 0
	s_lshr_b32 s90, s89, 8
	s_lshl_b32 s90, s90, 23
	s_lshl_b32 s91, s91, 19
	s_or_b32 s90, s90, s91
	s_bfe_u32 s91, s89, 0x40004
	s_lshl_b32 s91, s91, 7
	s_or_b32 s90, s90, s91
	s_lshl_b32 s91, s57, 15
	s_or_b32 s90, s90, s91
	s_add_u32 s90, s90, 0x4ee00000
	s_add_u32 s86, s48, s90
	s_addc_u32 s87, s49, 0
	global_load_dwordx4 v[180:183], v245, s[84:85] nt
	s_add_u32 s84, s84, 0x4000
	s_addc_u32 s85, s85, 0
	global_load_dwordx4 v[184:187], v245, s[84:85] nt
	s_add_u32 s84, s84, 0x4000
	s_addc_u32 s85, s85, 0
	global_load_dwordx4 v[188:191], v245, s[84:85] nt
	s_add_u32 s84, s84, 0x4000
	s_addc_u32 s85, s85, 0
	global_load_dwordx4 v[192:195], v245, s[84:85] nt
	s_add_u32 s84, s84, 0x4000
	s_addc_u32 s85, s85, 0
	global_load_dwordx4 v[196:199], v245, s[84:85] nt
	s_add_u32 s84, s84, 0x4000
	s_addc_u32 s85, s85, 0
	global_load_dwordx4 v[200:203], v245, s[84:85] nt
	s_add_u32 s84, s84, 0x4000
	s_addc_u32 s85, s85, 0
	global_load_dwordx4 v[204:207], v245, s[84:85] nt
	s_add_u32 s84, s84, 0x4000
	s_addc_u32 s85, s85, 0
	global_load_dwordx4 v[208:211], v245, s[84:85] nt
	s_add_u32 s84, s84, 0x4000
	s_addc_u32 s85, s85, 0
	global_load_dwordx4 v[212:215], v245, s[84:85] nt
	s_add_u32 s84, s84, 0x4000
	s_addc_u32 s85, s85, 0
	global_load_dwordx4 v[216:219], v245, s[84:85] nt
	s_add_u32 s84, s84, 0x4000
	s_addc_u32 s85, s85, 0
	global_load_dwordx4 v[220:223], v245, s[84:85] nt
	s_add_u32 s84, s84, 0x4000
	s_addc_u32 s85, s85, 0
	global_load_dwordx4 v[224:227], v245, s[84:85] nt
	s_add_u32 s84, s84, 0x4000
	s_addc_u32 s85, s85, 0
	global_load_dwordx4 v[228:231], v245, s[84:85] nt
	s_add_u32 s84, s84, 0x4000
	s_addc_u32 s85, s85, 0
	global_load_dwordx4 v[232:235], v245, s[84:85] nt
	s_add_u32 s84, s84, 0x4000
	s_addc_u32 s85, s85, 0
	global_load_dwordx4 v[236:239], v245, s[84:85] nt
	s_add_u32 s84, s84, 0x4000
	s_addc_u32 s85, s85, 0
	global_load_dwordx4 v[240:243], v245, s[84:85] nt

.LBB0_367:
	s_lshr_b32 s0, s56, 31
	s_add_i32 s0, s56, s0
	s_ashr_i32 s0, s0, 1
	v_readlane_b32 s78, v254, 5
	s_cmp_ge_i32 s78, s0
	v_readlane_b32 s79, v254, 8
	v_readlane_b32 s60, v254, 4
	s_cbranch_scc0 .LBB0_409
	s_sub_i32 s10, s78, s0
	s_cmpk_gt_u32 s10, 0x37f
	s_waitcnt vmcnt(0) lgkmcnt(0)
	s_barrier
	s_cbranch_scc1 .LBB0_409
	s_sub_i32 s0, s56, s0
	s_abs_i32 s2, s0
	v_cvt_f32_u32_e32 v2, s2
	s_sub_i32 s3, s0, s10
	s_add_i32 s4, s3, 0x37f
	s_sub_i32 s3, 0xfffffc81, s3
	v_rcp_iflag_f32_e32 v2, v2
	s_xor_b32 s6, s4, s0
	s_sub_i32 s5, 0, s2
	s_max_i32 s3, s4, s3
	v_mul_f32_e32 v2, 0x4f7ffffe, v2
	v_cvt_u32_f32_e32 v2, v2
	s_ashr_i32 s4, s6, 31
	s_add_i32 s1, s10, 0x2000
	v_readfirstlane_b32 s6, v2
	s_mul_i32 s5, s5, s6
	s_mul_hi_u32 s5, s6, s5
	s_add_i32 s6, s6, s5
	s_mul_hi_u32 s5, s3, s6
	s_mul_i32 s6, s5, s2
	s_sub_i32 s3, s3, s6
	s_add_i32 s7, s5, 1
	s_sub_i32 s6, s3, s2
	s_cmp_ge_u32 s3, s2
	s_cselect_b32 s5, s7, s5
	s_cselect_b32 s3, s6, s3
	s_add_i32 s6, s5, 1
	s_cmp_ge_u32 s3, s2
	s_cselect_b32 s2, s6, s5
	s_xor_b32 s2, s2, s4
	s_sub_i32 s18, s2, s4
	s_mov_b32 s18, 7
	s_movk_i32 s0, 0xff80
	s_lshl_b32 s12, s18, 2
	s_add_i32 s13, s12, -1
	s_cmp_gt_i32 s18, 0
	s_cselect_b64 s[2:3], -1, 0
	s_and_b64 s[4:5], s[2:3], exec
	s_cselect_b32 s11, 0, s13
	s_ashr_i32 s4, s11, 2
	s_mul_i32 s9, s4, s0
	s_add_i32 s9, s9, s1
	s_cmpk_gt_i32 s9, 0x1fff
	s_mov_b32 s5, 0
	s_cbranch_scc0 .LBB0_371
	s_add_i32 s4, s9, 0xffffe000
	s_lshr_b32 s4, s4, 7
	s_lshl_b64 s[4:5], s[4:5], 24
	v_readlane_b32 s34, v254, 13
	v_readlane_b32 s35, v254, 14
	s_add_u32 s6, s34, s4
	s_addc_u32 s7, s35, s5
	s_lshl_b32 s4, s9, 4
	s_and_b32 s19, s4, 0x780
	s_lshl_b32 s4, s9, 8
	v_readlane_b32 s30, v254, 11
	s_and_b32 s8, s4, 0x700
	v_readlane_b32 s31, v254, 12
	s_mov_b64 s[4:5], 0x800
	s_cbranch_execz .LBB0_372
	s_branch .LBB0_373

.LBB0_537:
	s_add_i32 s89, s58, -1
	s_cmp_lt_u32 s89, 2
	s_cselect_b32 s88, 1, 0
	s_cbranch_scc0 .Lp4c_skip1
	s_mul_i32 s89, s89, 256
	s_add_u32 s89, s89, s78
	s_add_u32 s89, s89, 6912
	s_cmp_lt_u32 s89, 0x2000
	s_cselect_b32 s88, 1, 0
	s_cbranch_scc0 .Lp4c_skip1
	s_lshr_b32 s90, s89, 4
	s_lshl_b32 s90, s90, 21
	s_and_b32 s91, s89, 15
	s_lshl_b32 s92, s91, 10
	s_or_b32 s90, s90, s92
	s_lshl_b32 s92, s57, 7
	s_or_b32 s90, s90, s92
	s_add_u32 s84, s82, s90
	s_addc_u32 s85, s83, 0
	s_lshr_b32 s90, s89, 8
	s_lshl_b32 s90, s90, 23
	s_lshl_b32 s91, s91, 19
	s_or_b32 s90, s90, s91
	s_bfe_u32 s91, s89, 0x40004
	s_lshl_b32 s91, s91, 7
	s_or_b32 s90, s90, s91
	s_lshl_b32 s91, s57, 15
	s_or_b32 s90, s90, s91
	s_add_u32 s90, s90, 0x4ee00000
	s_add_u32 s86, s48, s90
	s_addc_u32 s87, s49, 0
	global_load_dwordx4 v[180:183], v245, s[84:85] nt
	s_add_u32 s84, s84, 0x4000
	s_addc_u32 s85, s85, 0
	global_load_dwordx4 v[184:187], v245, s[84:85] nt
	s_add_u32 s84, s84, 0x4000
	s_addc_u32 s85, s85, 0
	global_load_dwordx4 v[188:191], v245, s[84:85] nt
	s_add_u32 s84, s84, 0x4000
	s_addc_u32 s85, s85, 0
	global_load_dwordx4 v[192:195], v245, s[84:85] nt
	s_add_u32 s84, s84, 0x4000
	s_addc_u32 s85, s85, 0
	global_load_dwordx4 v[196:199], v245, s[84:85] nt
	s_add_u32 s84, s84, 0x4000
	s_addc_u32 s85, s85, 0
	global_load_dwordx4 v[200:203], v245, s[84:85] nt
	s_add_u32 s84, s84, 0x4000
	s_addc_u32 s85, s85, 0
	global_load_dwordx4 v[204:207], v245, s[84:85] nt
	s_add_u32 s84, s84, 0x4000
	s_addc_u32 s85, s85, 0
	global_load_dwordx4 v[208:211], v245, s[84:85] nt
	s_add_u32 s84, s84, 0x4000
	s_addc_u32 s85, s85, 0
	global_load_dwordx4 v[212:215], v245, s[84:85] nt
	s_add_u32 s84, s84, 0x4000
	s_addc_u32 s85, s85, 0
	global_load_dwordx4 v[216:219], v245, s[84:85] nt
	s_add_u32 s84, s84, 0x4000
	s_addc_u32 s85, s85, 0
	global_load_dwordx4 v[220:223], v245, s[84:85] nt
	s_add_u32 s84, s84, 0x4000
	s_addc_u32 s85, s85, 0
	global_load_dwordx4 v[224:227], v245, s[84:85] nt
	s_add_u32 s84, s84, 0x4000
	s_addc_u32 s85, s85, 0
	global_load_dwordx4 v[228:231], v245, s[84:85] nt
	s_add_u32 s84, s84, 0x4000
	s_addc_u32 s85, s85, 0
	global_load_dwordx4 v[232:235], v245, s[84:85] nt
	s_add_u32 s84, s84, 0x4000
	s_addc_u32 s85, s85, 0
	global_load_dwordx4 v[236:239], v245, s[84:85] nt
	s_add_u32 s84, s84, 0x4000
	s_addc_u32 s85, s85, 0
	global_load_dwordx4 v[240:243], v245, s[84:85] nt

.LBB0_730:
	v_readlane_b32 s92, v254, 5
	s_nop 3
	s_lshl_b32 s93, s80, 8
	s_add_u32 s92, s92, s93
	s_add_u32 s92, s92, 128
	s_cmp_lt_u32 s92, 0x1000
	s_cselect_b32 s32, 1, 0
	s_cbranch_scc0 .Lp7c_skip1
	s_lshr_b32 s93, s92, 3
	s_lshl_b32 s93, s93, 20
	s_and_b32 s94, s92, 7
	s_lshl_b32 s95, s94, 10
	s_or_b32 s93, s93, s95
	s_lshl_b32 s95, s57, 7
	s_or_b32 s93, s93, s95
	s_add_u32 s90, s14, s93
	s_addc_u32 s91, s15, 0
	s_lshr_b32 s93, s92, 7
	s_lshl_b32 s93, s93, 22
	s_lshl_b32 s94, s94, 19
	s_or_b32 s93, s93, s94
	s_bfe_u32 s94, s92, 0x40003
	s_lshl_b32 s94, s94, 7
	s_or_b32 s93, s93, s94
	s_lshl_b32 s94, s57, 16
	s_or_b32 s93, s93, s94
	s_add_u32 s93, s93, 0x5ee00000
	s_add_u32 s88, s48, s93
	s_addc_u32 s89, s49, 0
	global_load_dwordx4 v[216:219], v249, s[90:91] nt
	s_add_u32 s90, s90, 0x2000
	s_addc_u32 s91, s91, 0
	global_load_dwordx4 v[220:223], v249, s[90:91] nt
	s_add_u32 s90, s90, 0x2000
	s_addc_u32 s91, s91, 0
	global_load_dwordx4 v[224:227], v249, s[90:91] nt
	s_add_u32 s90, s90, 0x2000
	s_addc_u32 s91, s91, 0
	global_load_dwordx4 v[228:231], v249, s[90:91] nt
	s_add_u32 s90, s90, 0x2000
	s_addc_u32 s91, s91, 0
	global_load_dwordx4 v[232:235], v249, s[90:91] nt
	s_add_u32 s90, s90, 0x2000
	s_addc_u32 s91, s91, 0
	global_load_dwordx4 v[236:239], v249, s[90:91] nt
	s_add_u32 s90, s90, 0x2000
	s_addc_u32 s91, s91, 0
	global_load_dwordx4 v[240:243], v249, s[90:91] nt
	s_add_u32 s90, s90, 0x2000
	s_addc_u32 s91, s91, 0
	global_load_dwordx4 v[244:247], v249, s[90:91] nt
	s_add_u32 s90, s90, 0x2000
	s_addc_u32 s91, s91, 0

.LBB0_741:
	s_or_b64 exec, exec, s[16:17]
	s_waitcnt lgkmcnt(0)
	s_barrier
	ds_read_b32 v6, v42
	s_mov_b64 s[16:17], -1
	s_waitcnt lgkmcnt(0)
	v_cmp_lt_i32_e32 vcc, s25, v6
	v_readfirstlane_b32 s4, v6
	s_cbranch_vccnz .LBB0_736
	s_add_i32 s18, s4, 0x2080
	s_cmpk_gt_i32 s4, 0xff7f
	s_cbranch_scc0 .LBB0_744
	s_addk_i32 s4, 0x80
	s_lshr_b32 s4, s4, 7
	s_lshl_b64 s[16:17], s[4:5], 22
	s_lshl_b64 s[20:21], s[4:5], 24
	s_add_u32 s19, s14, s20
	s_addc_u32 s21, s15, s21
	s_add_u32 s16, s22, s16
	s_addc_u32 s17, s23, s17
	s_lshl_b32 s20, s18, 8
	s_lshl_b32 s4, s18, 4
	s_and_b32 s27, s20, 0x700
	s_and_b32 s26, s4, 0x7f0
	s_and_b32 s4, s4, 0x780
	s_lshl_b32 s20, s27, 2
	s_add_u32 s20, s19, s20
	s_addc_u32 s21, s21, 0
	v_or_b32_e32 v43, s4, v8
	v_lshl_add_u64 v[6:7], s[20:21], 0, v[2:3]
	v_lshlrev_b32_e32 v44, 13, v43
	v_mov_b32_e32 v45, v3
	v_or_b32_e32 v43, s4, v9
	v_lshl_add_u64 v[52:53], v[6:7], 0, v[44:45]
	v_lshlrev_b32_e32 v44, 13, v43
	v_or_b32_e32 v43, s4, v11
	v_lshl_add_u64 v[54:55], v[6:7], 0, v[44:45]
	global_load_dwordx4 v[44:47], v[52:53], off
	global_load_dwordx4 v[48:51], v[54:55], off
	v_lshlrev_b32_e32 v52, 13, v43
	v_mov_b32_e32 v53, v3
	v_or_b32_e32 v43, s4, v13
	v_lshl_add_u64 v[60:61], v[6:7], 0, v[52:53]
	v_lshlrev_b32_e32 v52, 13, v43
	v_or_b32_e32 v43, s4, v15
	v_lshl_add_u64 v[62:63], v[6:7], 0, v[52:53]
	global_load_dwordx4 v[52:55], v[60:61], off
	global_load_dwordx4 v[56:59], v[62:63], off
	v_lshlrev_b32_e32 v60, 13, v43
	v_mov_b32_e32 v61, v3
	v_or_b32_e32 v43, s4, v17
	v_lshl_add_u64 v[68:69], v[6:7], 0, v[60:61]
	v_lshlrev_b32_e32 v60, 13, v43
	v_or_b32_e32 v43, s4, v19
	v_lshl_add_u64 v[70:71], v[6:7], 0, v[60:61]
	global_load_dwordx4 v[60:63], v[68:69], off
	global_load_dwordx4 v[64:67], v[70:71], off
	v_lshlrev_b32_e32 v68, 13, v43
	v_mov_b32_e32 v69, v3
	v_or_b32_e32 v43, s4, v21
	v_lshl_add_u64 v[76:77], v[6:7], 0, v[68:69]
	v_lshlrev_b32_e32 v68, 13, v43
	v_or_b32_e32 v43, s4, v23
	v_lshl_add_u64 v[78:79], v[6:7], 0, v[68:69]
	global_load_dwordx4 v[68:71], v[76:77], off
	global_load_dwordx4 v[72:75], v[78:79], off
	v_lshlrev_b32_e32 v76, 13, v43
	v_mov_b32_e32 v77, v3
	v_or_b32_e32 v43, s4, v25
	v_lshl_add_u64 v[84:85], v[6:7], 0, v[76:77]
	v_lshlrev_b32_e32 v76, 13, v43
	v_or_b32_e32 v43, s4, v27
	v_lshl_add_u64 v[86:87], v[6:7], 0, v[76:77]
	global_load_dwordx4 v[76:79], v[84:85], off
	global_load_dwordx4 v[80:83], v[86:87], off
	v_lshlrev_b32_e32 v84, 13, v43
	v_mov_b32_e32 v85, v3
	v_or_b32_e32 v43, s4, v29
	v_lshl_add_u64 v[92:93], v[6:7], 0, v[84:85]
	v_lshlrev_b32_e32 v84, 13, v43
	v_or_b32_e32 v43, s4, v31
	v_lshl_add_u64 v[94:95], v[6:7], 0, v[84:85]
	global_load_dwordx4 v[84:87], v[92:93], off
	global_load_dwordx4 v[88:91], v[94:95], off
	v_lshlrev_b32_e32 v92, 13, v43
	v_mov_b32_e32 v93, v3
	v_or_b32_e32 v43, s4, v33
	v_lshl_add_u64 v[100:101], v[6:7], 0, v[92:93]
	v_lshlrev_b32_e32 v92, 13, v43
	v_or_b32_e32 v43, s26, v35
	v_lshl_add_u64 v[102:103], v[6:7], 0, v[92:93]
	global_load_dwordx4 v[92:95], v[100:101], off
	global_load_dwordx4 v[96:99], v[102:103], off
	v_lshlrev_b32_e32 v100, 13, v43
	v_mov_b32_e32 v101, v3
	v_or_b32_e32 v43, s4, v37
	v_lshl_add_u64 v[108:109], v[6:7], 0, v[100:101]
	v_lshlrev_b32_e32 v100, 13, v43
	v_lshl_add_u64 v[6:7], v[6:7], 0, v[100:101]
	global_load_dwordx4 v[100:103], v[108:109], off
	global_load_dwordx4 v[104:107], v[6:7], off
	v_or_b32_e32 v6, s27, v39
	v_lshlrev_b32_e32 v6, 11, v6
	v_mov_b32_e32 v7, v3
	v_lshl_add_u64 v[6:7], s[16:17], 0, v[6:7]
	v_lshl_add_u64 v[6:7], v[6:7], 0, s[4:5]
	v_lshl_add_u64 v[6:7], v[6:7], 0, v[4:5]
	s_mov_b64 s[16:17], 0
	s_waitcnt vmcnt(15)
	ds_write_b128 v1, v[44:47]
	s_waitcnt vmcnt(14)
	ds_write_b128 v10, v[48:51]
	s_waitcnt vmcnt(13)
	ds_write_b128 v12, v[52:55]
	s_waitcnt vmcnt(12)
	ds_write_b128 v14, v[56:59]
	s_waitcnt vmcnt(11)
	ds_write_b128 v16, v[60:63]
	s_waitcnt vmcnt(10)
	ds_write_b128 v18, v[64:67]
	s_waitcnt vmcnt(9)
	ds_write_b128 v20, v[68:71]
	s_waitcnt vmcnt(8)
	ds_write_b128 v22, v[72:75]
	s_waitcnt vmcnt(7)
	ds_write_b128 v24, v[76:79] offset:64
	s_waitcnt vmcnt(6)
	ds_write_b128 v26, v[80:83] offset:64
	s_waitcnt vmcnt(5)
	ds_write_b128 v28, v[84:87] offset:64
	s_waitcnt vmcnt(4)
	ds_write_b128 v30, v[88:91] offset:64
	s_waitcnt vmcnt(3)
	ds_write_b128 v32, v[92:95] offset:64
	s_waitcnt vmcnt(2)
	ds_write_b128 v34, v[96:99] offset:64
	s_waitcnt vmcnt(1)
	ds_write_b128 v36, v[100:103] offset:64
	s_waitcnt vmcnt(0)
	ds_write_b128 v38, v[104:107]
	s_waitcnt lgkmcnt(0)
	s_barrier
	ds_read_b32 v43, v40
	ds_read_b32 v44, v40 offset:1040
	ds_read_b32 v45, v40 offset:2080
	ds_read_b32 v46, v40 offset:3120
	ds_read_b32 v47, v40 offset:4160
	ds_read_b32 v48, v40 offset:5200
	ds_read_b32 v49, v40 offset:6240
	ds_read_b32 v50, v40 offset:7280
	s_waitcnt lgkmcnt(6)
	v_mul_f32_e32 v51, 0x42000000, v44
	s_waitcnt lgkmcnt(5)
	v_mul_f32_e32 v52, 0x42000000, v45
	s_waitcnt lgkmcnt(4)
	v_mul_f32_e32 v53, 0x42000000, v46
	s_waitcnt lgkmcnt(3)
	v_mul_f32_e32 v46, 0x42000000, v47
	s_waitcnt lgkmcnt(2)
	v_mul_f32_e32 v47, 0x42000000, v48
	s_waitcnt lgkmcnt(1)
	v_mul_f32_e32 v48, 0x42000000, v49
	s_waitcnt lgkmcnt(0)
	v_mul_f32_e32 v49, 0x42000000, v50
	ds_read_b32 v44, v40 offset:8320
	ds_read_b32 v45, v40 offset:9360
	ds_read_b32 v50, v40 offset:10400
	ds_read_b32 v54, v40 offset:11440
	ds_read_b32 v55, v40 offset:12480
	ds_read_b32 v56, v40 offset:13520
	ds_read_b32 v57, v40 offset:14560
	ds_read_b32 v58, v40 offset:15600
	s_waitcnt lgkmcnt(6)
	v_mul_f32_e32 v60, 0x42000000, v45
	v_mov_b32_e32 v45, v3
	v_mul_f32_e32 v43, 0x42000000, v43
	v_mul_f32_e32 v59, 0x42000000, v44
	v_mov_b32_e32 v44, v3
	v_cvt_pk_fp8_f32 v45, v46, v47
	v_mov_b32_e32 v46, v3
	v_cvt_pk_fp8_f32 v44, v43, v51
	v_cvt_pk_fp8_f32 v46, v59, v60
	s_waitcnt lgkmcnt(5)
	v_mul_f32_e32 v50, 0x42000000, v50
	s_waitcnt lgkmcnt(4)
	v_mul_f32_e32 v54, 0x42000000, v54
	s_waitcnt lgkmcnt(3)
	v_mul_f32_e32 v55, 0x42000000, v55
	s_waitcnt lgkmcnt(2)
	v_mul_f32_e32 v56, 0x42000000, v56
	v_mov_b32_e32 v47, v3
	v_cvt_pk_fp8_f32 v44, v52, v53 op_sel:[0,0,1]
	v_cvt_pk_fp8_f32 v45, v48, v49 op_sel:[0,0,1]
	v_cvt_pk_fp8_f32 v46, v50, v54 op_sel:[0,0,1]
	ds_read_b32 v43, v40 offset:16640
	ds_read_b32 v48, v40 offset:17680
	ds_read_b32 v49, v40 offset:18720
	ds_read_b32 v50, v40 offset:19760
	ds_read_b32 v51, v40 offset:20800
	ds_read_b32 v52, v40 offset:21840
	ds_read_b32 v53, v40 offset:22880
	ds_read_b32 v54, v40 offset:23920
	v_cvt_pk_fp8_f32 v47, v55, v56
	s_waitcnt lgkmcnt(9)
	v_mul_f32_e32 v57, 0x42000000, v57
	s_waitcnt lgkmcnt(8)
	v_mul_f32_e32 v58, 0x42000000, v58
	s_waitcnt lgkmcnt(6)
	v_mul_f32_e32 v55, 0x42000000, v48
	v_cvt_pk_fp8_f32 v47, v57, v58 op_sel:[0,0,1]
	s_waitcnt lgkmcnt(5)
	v_mul_f32_e32 v56, 0x42000000, v49
	s_waitcnt lgkmcnt(4)
	v_mul_f32_e32 v57, 0x42000000, v50
	s_waitcnt lgkmcnt(3)
	v_mul_f32_e32 v50, 0x42000000, v51
	s_waitcnt lgkmcnt(2)
	v_mul_f32_e32 v51, 0x42000000, v52
	s_waitcnt lgkmcnt(1)
	v_mul_f32_e32 v52, 0x42000000, v53
	s_waitcnt lgkmcnt(0)
	v_mul_f32_e32 v53, 0x42000000, v54
	ds_read_b32 v48, v40 offset:24960
	ds_read_b32 v49, v40 offset:26000
	ds_read_b32 v54, v40 offset:27040
	ds_read_b32 v58, v40 offset:28080
	ds_read_b32 v59, v40 offset:29120
	ds_read_b32 v60, v40 offset:30160
	ds_read_b32 v61, v40 offset:31200
	ds_read_b32 v62, v40 offset:32240
	s_waitcnt lgkmcnt(6)
	v_mul_f32_e32 v64, 0x42000000, v49
	v_mov_b32_e32 v49, v3
	v_mul_f32_e32 v43, 0x42000000, v43
	v_mul_f32_e32 v63, 0x42000000, v48
	v_mov_b32_e32 v48, v3
	v_cvt_pk_fp8_f32 v49, v50, v51
	v_mov_b32_e32 v50, v3
	v_cvt_pk_fp8_f32 v48, v43, v55
	v_cvt_pk_fp8_f32 v50, v63, v64
	s_waitcnt lgkmcnt(5)
	v_mul_f32_e32 v54, 0x42000000, v54
	s_waitcnt lgkmcnt(4)
	v_mul_f32_e32 v58, 0x42000000, v58
	s_waitcnt lgkmcnt(3)
	v_mul_f32_e32 v59, 0x42000000, v59
	s_waitcnt lgkmcnt(2)
	v_mul_f32_e32 v60, 0x42000000, v60
	v_mov_b32_e32 v51, v3
	v_cvt_pk_fp8_f32 v48, v56, v57 op_sel:[0,0,1]
	v_cvt_pk_fp8_f32 v49, v52, v53 op_sel:[0,0,1]
	v_cvt_pk_fp8_f32 v50, v54, v58 op_sel:[0,0,1]
	ds_read_b32 v43, v40 offset:33280
	ds_read_b32 v52, v40 offset:34320
	ds_read_b32 v53, v40 offset:35360
	ds_read_b32 v54, v40 offset:36400
	ds_read_b32 v55, v40 offset:37440
	ds_read_b32 v56, v40 offset:38480
	ds_read_b32 v57, v40 offset:39520
	ds_read_b32 v58, v40 offset:40560
	v_cvt_pk_fp8_f32 v51, v59, v60
	s_waitcnt lgkmcnt(9)
	v_mul_f32_e32 v61, 0x42000000, v61
	s_waitcnt lgkmcnt(8)
	v_mul_f32_e32 v62, 0x42000000, v62
	s_waitcnt lgkmcnt(6)
	v_mul_f32_e32 v59, 0x42000000, v52
	v_cvt_pk_fp8_f32 v51, v61, v62 op_sel:[0,0,1]
	s_waitcnt lgkmcnt(5)
	v_mul_f32_e32 v60, 0x42000000, v53
	s_waitcnt lgkmcnt(4)
	v_mul_f32_e32 v61, 0x42000000, v54
	s_waitcnt lgkmcnt(3)
	v_mul_f32_e32 v54, 0x42000000, v55
	s_waitcnt lgkmcnt(2)
	v_mul_f32_e32 v55, 0x42000000, v56
	s_waitcnt lgkmcnt(1)
	v_mul_f32_e32 v56, 0x42000000, v57
	s_waitcnt lgkmcnt(0)
	v_mul_f32_e32 v57, 0x42000000, v58
	ds_read_b32 v52, v40 offset:41600
	ds_read_b32 v53, v40 offset:42640
	ds_read_b32 v58, v40 offset:43680
	ds_read_b32 v62, v40 offset:44720
	ds_read_b32 v63, v40 offset:45760
	ds_read_b32 v64, v40 offset:46800
	ds_read_b32 v65, v40 offset:47840
	ds_read_b32 v66, v40 offset:48880
	s_waitcnt lgkmcnt(6)
	v_mul_f32_e32 v68, 0x42000000, v53
	v_mov_b32_e32 v53, v3
	v_mul_f32_e32 v43, 0x42000000, v43
	v_mul_f32_e32 v67, 0x42000000, v52
	v_mov_b32_e32 v52, v3
	v_cvt_pk_fp8_f32 v53, v54, v55
	v_mov_b32_e32 v54, v3
	v_cvt_pk_fp8_f32 v52, v43, v59
	v_cvt_pk_fp8_f32 v54, v67, v68
	s_waitcnt lgkmcnt(5)
	v_mul_f32_e32 v58, 0x42000000, v58
	s_waitcnt lgkmcnt(4)
	v_mul_f32_e32 v62, 0x42000000, v62
	s_waitcnt lgkmcnt(3)
	v_mul_f32_e32 v63, 0x42000000, v63
	s_waitcnt lgkmcnt(2)
	v_mul_f32_e32 v64, 0x42000000, v64
	v_mov_b32_e32 v55, v3
	v_cvt_pk_fp8_f32 v52, v60, v61 op_sel:[0,0,1]
	v_cvt_pk_fp8_f32 v53, v56, v57 op_sel:[0,0,1]
	v_cvt_pk_fp8_f32 v54, v58, v62 op_sel:[0,0,1]
	ds_read_b32 v43, v40 offset:49920
	ds_read_b32 v56, v40 offset:50960
	ds_read_b32 v57, v40 offset:52000
	ds_read_b32 v58, v40 offset:53040
	ds_read_b32 v59, v40 offset:54080
	ds_read_b32 v60, v40 offset:55120
	ds_read_b32 v61, v40 offset:56160
	ds_read_b32 v62, v40 offset:57200
	v_cvt_pk_fp8_f32 v55, v63, v64
	s_waitcnt lgkmcnt(9)
	v_mul_f32_e32 v65, 0x42000000, v65
	s_waitcnt lgkmcnt(8)
	v_mul_f32_e32 v66, 0x42000000, v66
	s_waitcnt lgkmcnt(6)
	v_mul_f32_e32 v63, 0x42000000, v56
	v_cvt_pk_fp8_f32 v55, v65, v66 op_sel:[0,0,1]
	s_waitcnt lgkmcnt(5)
	v_mul_f32_e32 v64, 0x42000000, v57
	s_waitcnt lgkmcnt(4)
	v_mul_f32_e32 v65, 0x42000000, v58
	s_waitcnt lgkmcnt(3)
	v_mul_f32_e32 v58, 0x42000000, v59
	s_waitcnt lgkmcnt(2)
	v_mul_f32_e32 v59, 0x42000000, v60
	s_waitcnt lgkmcnt(1)
	v_mul_f32_e32 v60, 0x42000000, v61
	s_waitcnt lgkmcnt(0)
	v_mul_f32_e32 v61, 0x42000000, v62
	ds_read_b32 v56, v40 offset:58240
	ds_read_b32 v57, v40 offset:59280
	ds_read_b32 v62, v40 offset:60320
	ds_read_b32 v66, v40 offset:61360
	ds_read_b32 v67, v40 offset:62400
	ds_read_b32 v68, v40 offset:63440
	ds_read_b32 v69, v40 offset:64480
	ds_read_b32 v70, v40 offset:65520
	s_waitcnt lgkmcnt(6)
	v_mul_f32_e32 v72, 0x42000000, v57
	v_mov_b32_e32 v57, v3
	v_mul_f32_e32 v43, 0x42000000, v43
	v_mul_f32_e32 v71, 0x42000000, v56
	s_waitcnt lgkmcnt(3)
	v_mul_f32_e32 v67, 0x42000000, v67
	s_waitcnt lgkmcnt(2)
	v_mul_f32_e32 v68, 0x42000000, v68
	v_mov_b32_e32 v56, v3
	v_cvt_pk_fp8_f32 v57, v58, v59
	v_mov_b32_e32 v58, v3
	v_mov_b32_e32 v59, v3
	v_cvt_pk_fp8_f32 v56, v43, v63
	v_cvt_pk_fp8_f32 v58, v71, v72
	v_cvt_pk_fp8_f32 v59, v67, v68
	v_mul_f32_e32 v62, 0x42000000, v62
	v_mul_f32_e32 v66, 0x42000000, v66
	s_waitcnt lgkmcnt(1)
	v_mul_f32_e32 v69, 0x42000000, v69
	s_waitcnt lgkmcnt(0)
	v_mul_f32_e32 v70, 0x42000000, v70
	v_cvt_pk_fp8_f32 v56, v64, v65 op_sel:[0,0,1]
	v_cvt_pk_fp8_f32 v57, v60, v61 op_sel:[0,0,1]
	v_cvt_pk_fp8_f32 v58, v62, v66 op_sel:[0,0,1]
	v_cvt_pk_fp8_f32 v59, v69, v70 op_sel:[0,0,1]
	global_store_dwordx4 v[6:7], v[44:47], off
	global_store_dwordx4 v[6:7], v[48:51], off offset:16
	global_store_dwordx4 v[6:7], v[52:55], off offset:32
	global_store_dwordx4 v[6:7], v[56:59], off offset:48
	s_waitcnt lgkmcnt(0)
	s_barrier
